# speedup vs baseline: 1.0019x; 1.0019x over previous
.LBB0_17:
	v_sub_f32_e32 v2, v66, v244
	v_exp_f32_e32 v98, v2
	v_sub_f32_e32 v2, v50, v244
	v_exp_f32_e32 v82, v2
	v_sub_f32_e32 v2, v67, v244
	v_exp_f32_e32 v99, v2
	v_sub_f32_e32 v2, v51, v244
	v_exp_f32_e32 v83, v2
	v_sub_f32_e32 v2, v68, v244
	v_exp_f32_e32 v100, v2
	v_sub_f32_e32 v2, v52, v244
	v_exp_f32_e32 v84, v2
	v_sub_f32_e32 v2, v69, v244
	v_exp_f32_e32 v101, v2
	v_sub_f32_e32 v2, v53, v244
	v_exp_f32_e32 v85, v2
	v_sub_f32_e32 v2, v70, v244
	v_exp_f32_e32 v102, v2
	v_sub_f32_e32 v2, v54, v244
	v_exp_f32_e32 v86, v2
	v_sub_f32_e32 v2, v71, v244
	v_exp_f32_e32 v103, v2
	v_sub_f32_e32 v2, v55, v244
	v_exp_f32_e32 v87, v2
	v_sub_f32_e32 v2, v72, v244
	v_exp_f32_e32 v104, v2
	v_sub_f32_e32 v2, v56, v244
	v_exp_f32_e32 v88, v2
	v_sub_f32_e32 v2, v73, v244
	v_exp_f32_e32 v105, v2
	v_sub_f32_e32 v2, v57, v244
	v_exp_f32_e32 v89, v2
	v_sub_f32_e32 v2, v74, v244
	v_exp_f32_e32 v106, v2
	v_sub_f32_e32 v2, v58, v244
	v_exp_f32_e32 v90, v2
	v_sub_f32_e32 v2, v75, v244
	v_exp_f32_e32 v107, v2
	v_sub_f32_e32 v2, v59, v244
	v_exp_f32_e32 v91, v2
	v_sub_f32_e32 v2, v76, v244
	v_exp_f32_e32 v108, v2
	v_sub_f32_e32 v2, v60, v244
	v_exp_f32_e32 v92, v2
	v_sub_f32_e32 v2, v77, v244
	v_exp_f32_e32 v109, v2
	v_sub_f32_e32 v2, v61, v244
	v_exp_f32_e32 v93, v2
	v_sub_f32_e32 v2, v78, v244
	v_exp_f32_e32 v110, v2
	v_sub_f32_e32 v2, v62, v244
	v_exp_f32_e32 v94, v2
	v_sub_f32_e32 v2, v79, v244
	v_exp_f32_e32 v111, v2
	v_sub_f32_e32 v2, v63, v244
	v_exp_f32_e32 v95, v2
	v_sub_f32_e32 v2, v80, v244
	v_exp_f32_e32 v112, v2
	v_sub_f32_e32 v2, v64, v244
	v_exp_f32_e32 v96, v2
	v_sub_f32_e32 v2, v81, v244
	v_exp_f32_e32 v113, v2
	v_sub_f32_e32 v2, v65, v244
	v_exp_f32_e32 v97, v2
	s_andn2_b64 vcc, exec, s[4:5]
	s_mov_b32 s98, 1
	s_mov_b32 s97, 0
	s_cbranch_vccnz .LBB0_34
	v_mov_b32_e32 v2, v3
	v_mov_b64_e32 v[64:65], v[2:3]
	v_mov_b64_e32 v[80:81], v[2:3]
	s_sub_i32 s66, 0, s82
	s_movk_i32 s77, 0x4000
	v_mov_b32_e32 v243, 0
	s_mov_b32 s98, 2
	s_movk_i32 s99, 0xbb
	v_mov_b32_e32 v160, 0
	v_mov_b32_e32 v161, 0
	v_mov_b32_e32 v156, 0
	v_mov_b32_e32 v157, 0
	v_mov_b32_e32 v152, 0
	v_mov_b32_e32 v153, 0
	v_mov_b32_e32 v148, 0
	v_mov_b32_e32 v149, 0
	v_mov_b64_e32 v[62:63], v[2:3]
	v_mov_b64_e32 v[60:61], v[2:3]
	v_mov_b64_e32 v[58:59], v[2:3]
	v_mov_b64_e32 v[56:57], v[2:3]
	v_mov_b64_e32 v[54:55], v[2:3]
	v_mov_b64_e32 v[52:53], v[2:3]
	v_mov_b64_e32 v[50:51], v[2:3]
	v_mov_b64_e32 v[78:79], v[2:3]
	v_mov_b64_e32 v[76:77], v[2:3]
	v_mov_b64_e32 v[74:75], v[2:3]
	v_mov_b64_e32 v[72:73], v[2:3]
	v_mov_b64_e32 v[70:71], v[2:3]
	v_mov_b64_e32 v[68:69], v[2:3]
	v_mov_b64_e32 v[66:67], v[2:3]
	v_mov_b32_e32 v115, v114
	v_mov_b32_e32 v116, v114
	v_mov_b32_e32 v117, v114
	v_mov_b32_e32 v118, v114
	v_mov_b32_e32 v119, v114
	v_mov_b32_e32 v120, v114
	v_mov_b32_e32 v121, v114
	v_mov_b32_e32 v122, v114
	v_mov_b32_e32 v123, v114
	v_mov_b32_e32 v124, v114
	v_mov_b32_e32 v125, v114
	v_mov_b32_e32 v126, v114
	v_mov_b32_e32 v127, v114
	v_mov_b32_e32 v128, v114
	v_mov_b32_e32 v129, v114
	s_lshl_b32 s4, s76, 12
	s_lshl_b32 s5, s90, 2
	s_add_u32 s4, s4, s5
	s_add_u32 s100, s70, s4
	s_addc_u32 s101, s71, 0
	s_add_u32 s0, s74, s4
	s_addc_u32 s1, s75, 0
	s_sub_u32 s0, s0, 0x40000
	s_subb_u32 s1, s1, 0
	s_add_i32 s4, s98, 1
	s_min_i32 s4, s4, s95
	s_lshl_b32 s5, s4, 18
	s_add_u32 s18, s100, s5
	s_addc_u32 s19, s101, 0
	s_lshl_b32 s5, s98, 18
	s_add_u32 s20, s0, s5
	s_addc_u32 s21, s1, 0
	s_cmp_eq_u32 s4, s95
	s_cbranch_scc1 .Lclamp1p
	global_load_dwordx4 v[8:11], v245, s[18:19]
	global_load_dwordx4 v[4:7], v246, s[18:19]
	global_load_dwordx4 v[130:133], v245, s[20:21]
	global_load_dwordx4 v[12:15], v246, s[20:21]
